# v59 + MoE-down epilogue: later row blocks no longer wait vmcnt(0) for the previous block's store ack (row-list loads are covered by the first wait on each path)
# baseline (speedup 1.0000x reference)
; __device__ __forceinline__ unsigned pk4_fp8(float a, float b, float c, float d) { int w = 0; w = __builtin_amdgcn_cvt_pk_fp8_f32(clamp8(a), clamp8(b), w, false); w = __builtin_amdgcn_cvt_pk_fp8_f32(clamp8(c), clamp8(d), w, true); return (unsigned)w; }
;     __device__ __forceinline__ void operator()(AccRef acc, const GUnit& u, int wr, int wc, int fr, int fq) const {
;         const int e = u.x0, rt = u.x1, ct = u.x2, cnt = u.x3; const int* rl = rowlist + (size_t)e * ECAP; const int p0 = rt * 256 + wr * 64 + fr;
;         unsigned ent[2][4];
; #pragma unroll
;         for (int ai = 0; ai < 2; ++ai)
; #pragma unroll
;             for (int m = 0; m < 4; ++m) { int p = p0 + ai * 128 + m * 16; p = p < cnt ? p : cnt - 1; ent[ai][m] = (unsigned)rl[p]; }
; #pragma unroll
;         for (int ai = 0; ai < 2; ++ai)
; #pragma unroll
;             for (int m = 0; m < 4; ++m) { const int p = p0 + ai * 128 + m * 16;
;                 if (p < cnt) { u32x4 w;
; #pragma unroll
;                     for (int q = 0; q < 4; ++q) { const f32x4 v = acc[ai][q >> 1][m][q & 1] * (W8_INV * Y8_SCALE); w[q] = pk4_fp8(v[0], v[1], v[2], v[3]); }
;                     *(u32x4*)(Y + (size_t)ent[ai][m] * D + ct * 256 + wc * 64 + 16 * fq) = w; } }
.LBB0_1144:
	s_waitcnt lgkmcnt(0)
	v_pk_mul_f32 v[14:15], v[126:127], s[14:15] op_sel_hi:[1,0]
	v_pk_mul_f32 v[16:17], v[128:129], s[14:15] op_sel_hi:[1,0]
	v_med3_f32 v13, v14, s59, v193
	v_med3_f32 v15, v15, s59, v193
	v_mov_b32_e32 v14, v177
	v_cvt_pk_fp8_f32 v14, v13, v15
	v_med3_f32 v13, v16, s59, v193
	v_med3_f32 v15, v17, s59, v193
	v_pk_mul_f32 v[16:17], v[122:123], s[14:15] op_sel_hi:[1,0]
	v_cvt_pk_fp8_f32 v14, v13, v15 op_sel:[0,0,1]
	v_med3_f32 v13, v16, s59, v193
	v_med3_f32 v16, v17, s59, v193
	v_mov_b32_e32 v15, v177
	v_cvt_pk_fp8_f32 v15, v13, v16
	v_pk_mul_f32 v[16:17], v[124:125], s[14:15] op_sel_hi:[1,0]
	v_pk_mul_f32 v[18:19], v[120:121], s[14:15] op_sel_hi:[1,0]
	v_med3_f32 v13, v16, s59, v193
	v_med3_f32 v16, v17, s59, v193
	v_cvt_pk_fp8_f32 v15, v13, v16 op_sel:[0,0,1]
	v_pk_mul_f32 v[16:17], v[118:119], s[14:15] op_sel_hi:[1,0]
	s_nop 0
	v_med3_f32 v13, v16, s59, v193
	v_med3_f32 v17, v17, s59, v193
	v_mov_b32_e32 v16, v177
	v_cvt_pk_fp8_f32 v16, v13, v17
	v_med3_f32 v13, v18, s59, v193
	v_med3_f32 v17, v19, s59, v193
	v_pk_mul_f32 v[18:19], v[114:115], s[14:15] op_sel_hi:[1,0]
	v_cvt_pk_fp8_f32 v16, v13, v17 op_sel:[0,0,1]
	v_med3_f32 v13, v18, s59, v193
	v_med3_f32 v18, v19, s59, v193
	v_mov_b32_e32 v17, v177
	v_cvt_pk_fp8_f32 v17, v13, v18
	v_pk_mul_f32 v[18:19], v[116:117], s[14:15] op_sel_hi:[1,0]
	s_nop 0
	v_med3_f32 v13, v18, s59, v193
	v_med3_f32 v18, v19, s59, v193
	v_cvt_pk_fp8_f32 v17, v13, v18 op_sel:[0,0,1]
	v_mov_b32_e32 v13, v177
	v_lshlrev_b64 v[12:13], 11, v[12:13]
	v_lshl_add_u64 v[12:13], s[10:11], 0, v[12:13]
	v_lshl_add_u64 v[12:13], v[12:13], 0, s[22:23]
	v_lshl_add_u64 v[12:13], v[12:13], 0, s[6:7]
	v_lshl_add_u64 v[12:13], v[12:13], 0, v[162:163]
	global_store_dwordx4 v[12:13], v[14:17], off
	s_or_b64 exec, exec, s[24:25]
	v_cmp_gt_i32_e32 vcc, s48, v11
	s_and_saveexec_b64 s[24:25], vcc
	s_cbranch_execnz .LBB0_1153

; __device__ __forceinline__ unsigned pk4_fp8(float a, float b, float c, float d) { int w = 0; w = __builtin_amdgcn_cvt_pk_fp8_f32(clamp8(a), clamp8(b), w, false); w = __builtin_amdgcn_cvt_pk_fp8_f32(clamp8(c), clamp8(d), w, true); return (unsigned)w; }
;     __device__ __forceinline__ void operator()(AccRef acc, const GUnit& u, int wr, int wc, int fr, int fq) const {
;     ...
;             for (int m = 0; m < 4; ++m) { const int p = p0 + ai * 128 + m * 16;
;                 if (p < cnt) { u32x4 w;
; #pragma unroll
;                     for (int q = 0; q < 4; ++q) { const f32x4 v = acc[ai][q >> 1][m][q & 1] * (W8_INV * Y8_SCALE); w[q] = pk4_fp8(v[0], v[1], v[2], v[3]); }
;                     *(u32x4*)(Y + (size_t)ent[ai][m] * D + ct * 256 + wc * 64 + 16 * fq) = w; } }
.LBB0_1146:
	s_waitcnt lgkmcnt(0)
	v_pk_mul_f32 v[10:11], v[94:95], s[14:15] op_sel_hi:[1,0]
	v_pk_mul_f32 v[12:13], v[96:97], s[14:15] op_sel_hi:[1,0]
	v_med3_f32 v9, v10, s59, v193
	v_med3_f32 v11, v11, s59, v193
	v_mov_b32_e32 v10, v177
	v_cvt_pk_fp8_f32 v10, v9, v11
	v_med3_f32 v9, v12, s59, v193
	v_med3_f32 v11, v13, s59, v193
	v_pk_mul_f32 v[12:13], v[90:91], s[14:15] op_sel_hi:[1,0]
	v_cvt_pk_fp8_f32 v10, v9, v11 op_sel:[0,0,1]
	v_med3_f32 v9, v12, s59, v193
	v_med3_f32 v12, v13, s59, v193
	v_mov_b32_e32 v11, v177
	v_cvt_pk_fp8_f32 v11, v9, v12
	v_pk_mul_f32 v[12:13], v[92:93], s[14:15] op_sel_hi:[1,0]
	v_pk_mul_f32 v[14:15], v[88:89], s[14:15] op_sel_hi:[1,0]
	v_med3_f32 v9, v12, s59, v193
	v_med3_f32 v12, v13, s59, v193
	v_cvt_pk_fp8_f32 v11, v9, v12 op_sel:[0,0,1]
	v_pk_mul_f32 v[12:13], v[86:87], s[14:15] op_sel_hi:[1,0]
	s_nop 0
	v_med3_f32 v9, v12, s59, v193
	v_med3_f32 v13, v13, s59, v193
	v_mov_b32_e32 v12, v177
	v_cvt_pk_fp8_f32 v12, v9, v13
	v_med3_f32 v9, v14, s59, v193
	v_med3_f32 v13, v15, s59, v193
	v_pk_mul_f32 v[14:15], v[82:83], s[14:15] op_sel_hi:[1,0]
	v_cvt_pk_fp8_f32 v12, v9, v13 op_sel:[0,0,1]
	v_med3_f32 v9, v14, s59, v193
	v_med3_f32 v14, v15, s59, v193
	v_mov_b32_e32 v13, v177
	v_cvt_pk_fp8_f32 v13, v9, v14
	v_pk_mul_f32 v[14:15], v[84:85], s[14:15] op_sel_hi:[1,0]
	s_nop 0
	v_med3_f32 v9, v14, s59, v193
	v_med3_f32 v14, v15, s59, v193
	v_cvt_pk_fp8_f32 v13, v9, v14 op_sel:[0,0,1]
	v_mov_b32_e32 v9, v177
	v_lshlrev_b64 v[8:9], 11, v[8:9]
	v_lshl_add_u64 v[8:9], s[10:11], 0, v[8:9]
	v_lshl_add_u64 v[8:9], v[8:9], 0, s[22:23]
	v_lshl_add_u64 v[8:9], v[8:9], 0, s[6:7]
	v_lshl_add_u64 v[8:9], v[8:9], 0, v[162:163]
	global_store_dwordx4 v[8:9], v[10:13], off
	s_or_b64 exec, exec, s[24:25]
	v_cmp_gt_i32_e32 vcc, s48, v7
	s_and_saveexec_b64 s[24:25], vcc
	s_cbranch_execnz .LBB0_1155

; __device__ __forceinline__ unsigned pk4_fp8(float a, float b, float c, float d) { int w = 0; w = __builtin_amdgcn_cvt_pk_fp8_f32(clamp8(a), clamp8(b), w, false); w = __builtin_amdgcn_cvt_pk_fp8_f32(clamp8(c), clamp8(d), w, true); return (unsigned)w; }
;     __device__ __forceinline__ void operator()(AccRef acc, const GUnit& u, int wr, int wc, int fr, int fq) const {
;     ...
;             for (int m = 0; m < 4; ++m) { const int p = p0 + ai * 128 + m * 16;
;                 if (p < cnt) { u32x4 w;
; #pragma unroll
;                     for (int q = 0; q < 4; ++q) { const f32x4 v = acc[ai][q >> 1][m][q & 1] * (W8_INV * Y8_SCALE); w[q] = pk4_fp8(v[0], v[1], v[2], v[3]); }
;                     *(u32x4*)(Y + (size_t)ent[ai][m] * D + ct * 256 + wc * 64 + 16 * fq) = w; } }
.LBB0_1148:
	s_waitcnt lgkmcnt(0)
	v_pk_mul_f32 v[6:7], v[62:63], s[14:15] op_sel_hi:[1,0]
	v_pk_mul_f32 v[8:9], v[64:65], s[14:15] op_sel_hi:[1,0]
	v_med3_f32 v5, v6, s59, v193
	v_med3_f32 v7, v7, s59, v193
	v_mov_b32_e32 v6, v177
	v_cvt_pk_fp8_f32 v6, v5, v7
	v_med3_f32 v5, v8, s59, v193
	v_med3_f32 v7, v9, s59, v193
	v_pk_mul_f32 v[8:9], v[58:59], s[14:15] op_sel_hi:[1,0]
	v_cvt_pk_fp8_f32 v6, v5, v7 op_sel:[0,0,1]
	v_med3_f32 v5, v8, s59, v193
	v_med3_f32 v8, v9, s59, v193
	v_mov_b32_e32 v7, v177
	v_cvt_pk_fp8_f32 v7, v5, v8
	v_pk_mul_f32 v[8:9], v[60:61], s[14:15] op_sel_hi:[1,0]
	v_pk_mul_f32 v[10:11], v[56:57], s[14:15] op_sel_hi:[1,0]
	v_med3_f32 v5, v8, s59, v193
	v_med3_f32 v8, v9, s59, v193
	v_cvt_pk_fp8_f32 v7, v5, v8 op_sel:[0,0,1]
	v_pk_mul_f32 v[8:9], v[54:55], s[14:15] op_sel_hi:[1,0]
	s_nop 0
	v_med3_f32 v5, v8, s59, v193
	v_med3_f32 v9, v9, s59, v193
	v_mov_b32_e32 v8, v177
	v_cvt_pk_fp8_f32 v8, v5, v9
	v_med3_f32 v5, v10, s59, v193
	v_med3_f32 v9, v11, s59, v193
	v_pk_mul_f32 v[10:11], v[50:51], s[14:15] op_sel_hi:[1,0]
	v_cvt_pk_fp8_f32 v8, v5, v9 op_sel:[0,0,1]
	v_med3_f32 v5, v10, s59, v193
	v_med3_f32 v10, v11, s59, v193
	v_mov_b32_e32 v9, v177
	v_cvt_pk_fp8_f32 v9, v5, v10
	v_pk_mul_f32 v[10:11], v[52:53], s[14:15] op_sel_hi:[1,0]
	s_nop 0
	v_med3_f32 v5, v10, s59, v193
	v_med3_f32 v10, v11, s59, v193
	v_cvt_pk_fp8_f32 v9, v5, v10 op_sel:[0,0,1]
	v_mov_b32_e32 v5, v177
	v_lshlrev_b64 v[4:5], 11, v[4:5]
	v_lshl_add_u64 v[4:5], s[10:11], 0, v[4:5]
	v_lshl_add_u64 v[4:5], v[4:5], 0, s[22:23]
	v_lshl_add_u64 v[4:5], v[4:5], 0, s[6:7]
	v_lshl_add_u64 v[4:5], v[4:5], 0, v[162:163]
	global_store_dwordx4 v[4:5], v[6:9], off
	s_or_b64 exec, exec, s[24:25]
	v_cmp_gt_i32_e32 vcc, s48, v3
	s_and_saveexec_b64 s[24:25], vcc
	s_cbranch_execnz .LBB0_1157

; __device__ __forceinline__ unsigned pk4_fp8(float a, float b, float c, float d) { int w = 0; w = __builtin_amdgcn_cvt_pk_fp8_f32(clamp8(a), clamp8(b), w, false); w = __builtin_amdgcn_cvt_pk_fp8_f32(clamp8(c), clamp8(d), w, true); return (unsigned)w; }
;     __device__ __forceinline__ void operator()(AccRef acc, const GUnit& u, int wr, int wc, int fr, int fq) const {
;     ...
;             for (int m = 0; m < 4; ++m) { int p = p0 + ai * 128 + m * 16; p = p < cnt ? p : cnt - 1; ent[ai][m] = (unsigned)rl[p]; }
; #pragma unroll
;         for (int ai = 0; ai < 2; ++ai)
; #pragma unroll
;             for (int m = 0; m < 4; ++m) { const int p = p0 + ai * 128 + m * 16;
;                 if (p < cnt) { u32x4 w;
; #pragma unroll
;                     for (int q = 0; q < 4; ++q) { const f32x4 v = acc[ai][q >> 1][m][q & 1] * (W8_INV * Y8_SCALE); w[q] = pk4_fp8(v[0], v[1], v[2], v[3]); }
;                     *(u32x4*)(Y + (size_t)ent[ai][m] * D + ct * 256 + wc * 64 + 16 * fq) = w; } }
.LBB0_1150:
	s_waitcnt vmcnt(0)
	s_or_b64 exec, exec, s[24:25]
	v_cmp_gt_i32_e32 vcc, s48, v15
	s_and_saveexec_b64 s[24:25], vcc
	s_cbranch_execz .LBB0_1143
.LBB0_1151:
	v_pk_mul_f32 v[16:17], v[142:143], s[14:15] op_sel_hi:[1,0]
	v_pk_mul_f32 v[18:19], v[144:145], s[14:15] op_sel_hi:[1,0]
	v_med3_f32 v15, v16, s59, v193
	v_med3_f32 v17, v17, s59, v193
	v_mov_b32_e32 v16, v177
	v_cvt_pk_fp8_f32 v16, v15, v17
	v_med3_f32 v15, v18, s59, v193
	v_med3_f32 v17, v19, s59, v193
	v_pk_mul_f32 v[18:19], v[138:139], s[14:15] op_sel_hi:[1,0]
	v_cvt_pk_fp8_f32 v16, v15, v17 op_sel:[0,0,1]
	v_med3_f32 v15, v18, s59, v193
	v_med3_f32 v18, v19, s59, v193
	v_mov_b32_e32 v17, v177
	v_cvt_pk_fp8_f32 v17, v15, v18
	v_pk_mul_f32 v[18:19], v[140:141], s[14:15] op_sel_hi:[1,0]
	v_pk_mul_f32 v[20:21], v[136:137], s[14:15] op_sel_hi:[1,0]
	v_med3_f32 v15, v18, s59, v193
	v_med3_f32 v18, v19, s59, v193
	v_cvt_pk_fp8_f32 v17, v15, v18 op_sel:[0,0,1]
	v_pk_mul_f32 v[18:19], v[134:135], s[14:15] op_sel_hi:[1,0]
	s_nop 0
	v_med3_f32 v15, v18, s59, v193
	v_med3_f32 v19, v19, s59, v193
	v_mov_b32_e32 v18, v177
	v_cvt_pk_fp8_f32 v18, v15, v19
	v_med3_f32 v15, v20, s59, v193
	v_med3_f32 v19, v21, s59, v193
	v_pk_mul_f32 v[20:21], v[130:131], s[14:15] op_sel_hi:[1,0]
	v_cvt_pk_fp8_f32 v18, v15, v19 op_sel:[0,0,1]
	v_med3_f32 v15, v20, s59, v193
	v_med3_f32 v20, v21, s59, v193
	v_mov_b32_e32 v19, v177
	v_cvt_pk_fp8_f32 v19, v15, v20
	v_pk_mul_f32 v[20:21], v[132:133], s[14:15] op_sel_hi:[1,0]
	s_nop 0
	v_med3_f32 v15, v20, s59, v193
	v_med3_f32 v20, v21, s59, v193
	v_cvt_pk_fp8_f32 v19, v15, v20 op_sel:[0,0,1]
	v_mov_b32_e32 v15, v177
	s_waitcnt lgkmcnt(0)
	v_lshlrev_b64 v[14:15], 11, v[14:15]
	v_lshl_add_u64 v[14:15], s[10:11], 0, v[14:15]
	v_lshl_add_u64 v[14:15], v[14:15], 0, s[22:23]
	v_lshl_add_u64 v[14:15], v[14:15], 0, s[6:7]
	v_lshl_add_u64 v[14:15], v[14:15], 0, v[162:163]
	global_store_dwordx4 v[14:15], v[16:19], off
	s_or_b64 exec, exec, s[24:25]
	v_cmp_gt_i32_e32 vcc, s48, v13
	s_and_saveexec_b64 s[24:25], vcc
	s_cbranch_execnz .LBB0_1144

; __device__ __forceinline__ unsigned pk4_fp8(float a, float b, float c, float d) { int w = 0; w = __builtin_amdgcn_cvt_pk_fp8_f32(clamp8(a), clamp8(b), w, false); w = __builtin_amdgcn_cvt_pk_fp8_f32(clamp8(c), clamp8(d), w, true); return (unsigned)w; }
;     __device__ __forceinline__ void operator()(AccRef acc, const GUnit& u, int wr, int wc, int fr, int fq) const {
;     ...
;             for (int m = 0; m < 4; ++m) { const int p = p0 + ai * 128 + m * 16;
;                 if (p < cnt) { u32x4 w;
; #pragma unroll
;                     for (int q = 0; q < 4; ++q) { const f32x4 v = acc[ai][q >> 1][m][q & 1] * (W8_INV * Y8_SCALE); w[q] = pk4_fp8(v[0], v[1], v[2], v[3]); }
;                     *(u32x4*)(Y + (size_t)ent[ai][m] * D + ct * 256 + wc * 64 + 16 * fq) = w; } }
.LBB0_1153:
	s_waitcnt lgkmcnt(0)
	v_pk_mul_f32 v[12:13], v[110:111], s[14:15] op_sel_hi:[1,0]
	v_pk_mul_f32 v[14:15], v[112:113], s[14:15] op_sel_hi:[1,0]
	v_med3_f32 v11, v12, s59, v193
	v_med3_f32 v13, v13, s59, v193
	v_mov_b32_e32 v12, v177
	v_cvt_pk_fp8_f32 v12, v11, v13
	v_med3_f32 v11, v14, s59, v193
	v_med3_f32 v13, v15, s59, v193
	v_pk_mul_f32 v[14:15], v[106:107], s[14:15] op_sel_hi:[1,0]
	v_cvt_pk_fp8_f32 v12, v11, v13 op_sel:[0,0,1]
	v_med3_f32 v11, v14, s59, v193
	v_med3_f32 v14, v15, s59, v193
	v_mov_b32_e32 v13, v177
	v_cvt_pk_fp8_f32 v13, v11, v14
	v_pk_mul_f32 v[14:15], v[108:109], s[14:15] op_sel_hi:[1,0]
	v_pk_mul_f32 v[16:17], v[104:105], s[14:15] op_sel_hi:[1,0]
	v_med3_f32 v11, v14, s59, v193
	v_med3_f32 v14, v15, s59, v193
	v_cvt_pk_fp8_f32 v13, v11, v14 op_sel:[0,0,1]
	v_pk_mul_f32 v[14:15], v[102:103], s[14:15] op_sel_hi:[1,0]
	s_nop 0
	v_med3_f32 v11, v14, s59, v193
	v_med3_f32 v15, v15, s59, v193
	v_mov_b32_e32 v14, v177
	v_cvt_pk_fp8_f32 v14, v11, v15
	v_med3_f32 v11, v16, s59, v193
	v_med3_f32 v15, v17, s59, v193
	v_pk_mul_f32 v[16:17], v[98:99], s[14:15] op_sel_hi:[1,0]
	v_cvt_pk_fp8_f32 v14, v11, v15 op_sel:[0,0,1]
	v_med3_f32 v11, v16, s59, v193
	v_med3_f32 v16, v17, s59, v193
	v_mov_b32_e32 v15, v177
	v_cvt_pk_fp8_f32 v15, v11, v16
	v_pk_mul_f32 v[16:17], v[100:101], s[14:15] op_sel_hi:[1,0]
	s_nop 0
	v_med3_f32 v11, v16, s59, v193
	v_med3_f32 v16, v17, s59, v193
	v_cvt_pk_fp8_f32 v15, v11, v16 op_sel:[0,0,1]
	v_mov_b32_e32 v11, v177
	v_lshlrev_b64 v[10:11], 11, v[10:11]
	v_lshl_add_u64 v[10:11], s[10:11], 0, v[10:11]
	v_lshl_add_u64 v[10:11], v[10:11], 0, s[22:23]
	v_lshl_add_u64 v[10:11], v[10:11], 0, s[6:7]
	v_lshl_add_u64 v[10:11], v[10:11], 0, v[162:163]
	global_store_dwordx4 v[10:11], v[12:15], off
	s_or_b64 exec, exec, s[24:25]
	v_cmp_gt_i32_e32 vcc, s48, v9
	s_and_saveexec_b64 s[24:25], vcc
	s_cbranch_execnz .LBB0_1146

; __device__ __forceinline__ unsigned pk4_fp8(float a, float b, float c, float d) { int w = 0; w = __builtin_amdgcn_cvt_pk_fp8_f32(clamp8(a), clamp8(b), w, false); w = __builtin_amdgcn_cvt_pk_fp8_f32(clamp8(c), clamp8(d), w, true); return (unsigned)w; }
;     __device__ __forceinline__ void operator()(AccRef acc, const GUnit& u, int wr, int wc, int fr, int fq) const {
;     ...
;             for (int m = 0; m < 4; ++m) { const int p = p0 + ai * 128 + m * 16;
;                 if (p < cnt) { u32x4 w;
; #pragma unroll
;                     for (int q = 0; q < 4; ++q) { const f32x4 v = acc[ai][q >> 1][m][q & 1] * (W8_INV * Y8_SCALE); w[q] = pk4_fp8(v[0], v[1], v[2], v[3]); }
;                     *(u32x4*)(Y + (size_t)ent[ai][m] * D + ct * 256 + wc * 64 + 16 * fq) = w; } }
.LBB0_1155:
	s_waitcnt lgkmcnt(0)
	v_pk_mul_f32 v[8:9], v[78:79], s[14:15] op_sel_hi:[1,0]
	v_pk_mul_f32 v[10:11], v[80:81], s[14:15] op_sel_hi:[1,0]
	v_med3_f32 v7, v8, s59, v193
	v_med3_f32 v9, v9, s59, v193
	v_mov_b32_e32 v8, v177
	v_cvt_pk_fp8_f32 v8, v7, v9
	v_med3_f32 v7, v10, s59, v193
	v_med3_f32 v9, v11, s59, v193
	v_pk_mul_f32 v[10:11], v[74:75], s[14:15] op_sel_hi:[1,0]
	v_cvt_pk_fp8_f32 v8, v7, v9 op_sel:[0,0,1]
	v_med3_f32 v7, v10, s59, v193
	v_med3_f32 v10, v11, s59, v193
	v_mov_b32_e32 v9, v177
	v_cvt_pk_fp8_f32 v9, v7, v10
	v_pk_mul_f32 v[10:11], v[76:77], s[14:15] op_sel_hi:[1,0]
	v_pk_mul_f32 v[12:13], v[72:73], s[14:15] op_sel_hi:[1,0]
	v_med3_f32 v7, v10, s59, v193
	v_med3_f32 v10, v11, s59, v193
	v_cvt_pk_fp8_f32 v9, v7, v10 op_sel:[0,0,1]
	v_pk_mul_f32 v[10:11], v[70:71], s[14:15] op_sel_hi:[1,0]
	s_nop 0
	v_med3_f32 v7, v10, s59, v193
	v_med3_f32 v11, v11, s59, v193
	v_mov_b32_e32 v10, v177
	v_cvt_pk_fp8_f32 v10, v7, v11
	v_med3_f32 v7, v12, s59, v193
	v_med3_f32 v11, v13, s59, v193
	v_pk_mul_f32 v[12:13], v[66:67], s[14:15] op_sel_hi:[1,0]
	v_cvt_pk_fp8_f32 v10, v7, v11 op_sel:[0,0,1]
	v_med3_f32 v7, v12, s59, v193
	v_med3_f32 v12, v13, s59, v193
	v_mov_b32_e32 v11, v177
	v_cvt_pk_fp8_f32 v11, v7, v12
	v_pk_mul_f32 v[12:13], v[68:69], s[14:15] op_sel_hi:[1,0]
	s_nop 0
	v_med3_f32 v7, v12, s59, v193
	v_med3_f32 v12, v13, s59, v193
	v_cvt_pk_fp8_f32 v11, v7, v12 op_sel:[0,0,1]
	v_mov_b32_e32 v7, v177
	v_lshlrev_b64 v[6:7], 11, v[6:7]
	v_lshl_add_u64 v[6:7], s[10:11], 0, v[6:7]
	v_lshl_add_u64 v[6:7], v[6:7], 0, s[22:23]
	v_lshl_add_u64 v[6:7], v[6:7], 0, s[6:7]
	v_lshl_add_u64 v[6:7], v[6:7], 0, v[162:163]
	global_store_dwordx4 v[6:7], v[8:11], off
	s_or_b64 exec, exec, s[24:25]
	v_cmp_gt_i32_e32 vcc, s48, v5
	s_and_saveexec_b64 s[24:25], vcc
	s_cbranch_execnz .LBB0_1148

; __device__ __forceinline__ unsigned pk4_fp8(float a, float b, float c, float d) { int w = 0; w = __builtin_amdgcn_cvt_pk_fp8_f32(clamp8(a), clamp8(b), w, false); w = __builtin_amdgcn_cvt_pk_fp8_f32(clamp8(c), clamp8(d), w, true); return (unsigned)w; }
; template <class Epi, class Sched, bool ALIGN_EPI = true, bool F8 = false>
; __device__ __forceinline__ void gemm_phase(PG8_LAS unsigned char* lds, const Sched& S, const Epi& E) {
;     ...
;         if (!has_next) break;
;     __device__ __forceinline__ void operator()(AccRef acc, const GUnit& u, int wr, int wc, int fr, int fq) const {
;     ...
;             for (int m = 0; m < 4; ++m) { const int p = p0 + ai * 128 + m * 16;
;                 if (p < cnt) { u32x4 w;
; #pragma unroll
;                     for (int q = 0; q < 4; ++q) { const f32x4 v = acc[ai][q >> 1][m][q & 1] * (W8_INV * Y8_SCALE); w[q] = pk4_fp8(v[0], v[1], v[2], v[3]); }
;                     *(u32x4*)(Y + (size_t)ent[ai][m] * D + ct * 256 + wc * 64 + 16 * fq) = w; } }
.LBB0_1157:
	s_waitcnt lgkmcnt(0)
	v_pk_mul_f32 v[4:5], v[46:47], s[14:15] op_sel_hi:[1,0]
	v_pk_mul_f32 v[6:7], v[48:49], s[14:15] op_sel_hi:[1,0]
	v_med3_f32 v3, v4, s59, v193
	v_med3_f32 v5, v5, s59, v193
	v_mov_b32_e32 v4, v177
	v_cvt_pk_fp8_f32 v4, v3, v5
	v_med3_f32 v3, v6, s59, v193
	v_med3_f32 v5, v7, s59, v193
	v_pk_mul_f32 v[6:7], v[42:43], s[14:15] op_sel_hi:[1,0]
	v_cvt_pk_fp8_f32 v4, v3, v5 op_sel:[0,0,1]
	v_med3_f32 v3, v6, s59, v193
	v_med3_f32 v6, v7, s59, v193
	v_mov_b32_e32 v5, v177
	v_cvt_pk_fp8_f32 v5, v3, v6
	v_pk_mul_f32 v[6:7], v[44:45], s[14:15] op_sel_hi:[1,0]
	v_pk_mul_f32 v[8:9], v[40:41], s[14:15] op_sel_hi:[1,0]
	v_med3_f32 v3, v6, s59, v193
	v_med3_f32 v6, v7, s59, v193
	v_cvt_pk_fp8_f32 v5, v3, v6 op_sel:[0,0,1]
	v_pk_mul_f32 v[6:7], v[38:39], s[14:15] op_sel_hi:[1,0]
	s_nop 0
	v_med3_f32 v3, v6, s59, v193
	v_med3_f32 v7, v7, s59, v193
	v_mov_b32_e32 v6, v177
	v_cvt_pk_fp8_f32 v6, v3, v7
	v_med3_f32 v3, v8, s59, v193
	v_med3_f32 v7, v9, s59, v193
	v_pk_mul_f32 v[8:9], v[34:35], s[14:15] op_sel_hi:[1,0]
	v_cvt_pk_fp8_f32 v6, v3, v7 op_sel:[0,0,1]
	v_med3_f32 v3, v8, s59, v193
	v_med3_f32 v8, v9, s59, v193
	v_mov_b32_e32 v7, v177
	v_cvt_pk_fp8_f32 v7, v3, v8
	v_pk_mul_f32 v[8:9], v[36:37], s[14:15] op_sel_hi:[1,0]
	s_nop 0
	v_med3_f32 v3, v8, s59, v193
	v_med3_f32 v8, v9, s59, v193
	v_cvt_pk_fp8_f32 v7, v3, v8 op_sel:[0,0,1]
	v_mov_b32_e32 v3, v177
	v_lshlrev_b64 v[2:3], 11, v[2:3]
	v_lshl_add_u64 v[2:3], s[10:11], 0, v[2:3]
	v_lshl_add_u64 v[2:3], v[2:3], 0, s[22:23]
	v_lshl_add_u64 v[2:3], v[2:3], 0, s[6:7]
	v_lshl_add_u64 v[2:3], v[2:3], 0, v[162:163]
	global_store_dwordx4 v[2:3], v[4:7], off
	s_or_b64 exec, exec, s[24:25]
	s_andn2_b64 vcc, exec, s[20:21]
	s_mov_b64 s[20:21], -1
	s_cbranch_vccnz .LBB0_1132
